# counted vmcnt waits (2 tiles in flight) in the expert-weight fp8 conversion loop of the conv role
# speedup vs baseline: 1.0208x; 1.0208x over previous
.LBB0_657:
	s_add_i32 s11, s4, -1
	s_and_b32 s11, s24, s11
	s_ff1_i32_b32 s4, s4
	s_lshl_b32 s25, s11, 6
	s_lshr_b32 s4, s24, s4
	s_lshl_b32 s24, s24, 10
	s_lshl_b32 s11, s11, 5
	s_and_b32 s24, s24, 0x800
	s_and_b32 s11, s11, 0x3f80
	v_bitop3_b32 v67, s25, v108, v1 bitop3:0xc8
	s_add_i32 s11, s11, s24
	v_or_b32_e32 v66, s25, v1
	v_or_b32_e32 v67, s11, v67
	v_cndmask_b32_e64 v100, v66, v67, s[0:1]
	v_lshl_add_u32 v66, s4, 8, v102
	v_mad_i64_i32 v[66:67], s[0:1], s10, v66, 0
	v_lshl_add_u64 v[66:67], v[66:67], 2, s[8:9]
	v_lshl_add_u64 v[66:67], v[100:101], 2, v[66:67]
	s_lshl_b32 s4, s10, 2
	v_lshl_add_u64 v[74:75], v[66:67], 0, s[4:5]
	global_load_dwordx4 v[66:69], v[66:67], off nt
	s_nop 0
	global_load_dwordx4 v[70:73], v[74:75], off nt
	v_lshl_add_u64 v[74:75], v[74:75], 0, s[4:5]
	v_lshl_add_u64 v[82:83], v[74:75], 0, s[4:5]
	global_load_dwordx4 v[74:77], v[74:75], off nt
	s_nop 0
	global_load_dwordx4 v[78:81], v[82:83], off nt
	v_lshl_add_u64 v[82:83], v[82:83], 0, s[4:5]
	v_lshl_add_u64 v[90:91], v[82:83], 0, s[4:5]
	global_load_dwordx4 v[82:85], v[82:83], off nt
	s_nop 0
	global_load_dwordx4 v[86:89], v[90:91], off nt
	v_lshl_add_u64 v[90:91], v[90:91], 0, s[4:5]
	v_lshl_add_u64 v[94:95], v[90:91], 0, s[4:5]
	global_load_dwordx4 v[90:93], v[90:91], off nt
	s_nop 0
	global_load_dwordx4 v[94:97], v[94:95], off nt
	s_waitcnt vmcnt(16)
	s_branch .LBB0_658
.Lmy_c1_skip:
	s_waitcnt vmcnt(0)
.LBB0_658:
	s_add_i32 s4, s89, s3
	s_sub_i32 s11, s4, 40
	s_cmpk_gt_i32 s11, 0x3fff
	s_mov_b64 s[8:9], -1
	s_cbranch_scc0 .LBB0_660
	s_addk_i32 s4, 0xbfd8
	s_lshr_b32 s4, s4, 8
	s_and_b32 s10, s11, 0xff
	s_lshl_b64 s[0:1], s[4:5], 22
	s_add_u32 s0, s13, s0
	s_addc_u32 s1, s14, s1
	s_mov_b64 s[8:9], 0

.LBB0_662:
	v_mul_f32_e32 v100, 0x42800000, v6
	v_mul_f32_e32 v111, 0x42800000, v2
	v_mov_b32_e32 v110, 0
	v_cvt_pk_fp8_f32 v110, v100, v111
	v_mul_f32_e32 v100, 0x42800000, v26
	v_mul_f32_e32 v114, 0x42800000, v22
	v_mov_b32_e32 v111, 0
	v_cvt_pk_fp8_f32 v111, v100, v114
	v_mul_f32_e32 v112, 0x42800000, v18
	v_mul_f32_e32 v113, 0x42800000, v10
	v_cvt_pk_fp8_f32 v110, v112, v113 op_sel:[0,0,1]
	v_mul_f32_e32 v100, 0x42800000, v30
	v_mul_f32_e32 v112, 0x42800000, v14
	v_cvt_pk_fp8_f32 v111, v100, v112 op_sel:[0,0,1]
	v_mul_f32_e32 v100, 0x42800000, v7
	v_mul_f32_e32 v112, 0x42800000, v3
	v_mov_b32_e32 v115, 0
	v_cvt_pk_fp8_f32 v115, v100, v112
	v_mul_f32_e32 v100, 0x42800000, v27
	v_mul_f32_e32 v112, 0x42800000, v23
	v_mov_b32_e32 v116, 0
	v_cvt_pk_fp8_f32 v116, v100, v112
	v_mul_f32_e32 v113, 0x42800000, v19
	v_mul_f32_e32 v114, 0x42800000, v11
	v_mul_f32_e32 v100, 0x42800000, v31
	v_mul_f32_e32 v112, 0x42800000, v15
	v_cvt_pk_fp8_f32 v115, v113, v114 op_sel:[0,0,1]
	v_cvt_pk_fp8_f32 v116, v100, v112 op_sel:[0,0,1]
	v_mul_f32_e32 v100, 0x42800000, v8
	v_mul_f32_e32 v113, 0x42800000, v4
	v_mov_b32_e32 v112, 0
	v_cvt_pk_fp8_f32 v112, v100, v113
	v_mul_f32_e32 v100, 0x42800000, v28
	v_mul_f32_e32 v118, 0x42800000, v24
	v_mov_b32_e32 v113, 0
	v_cvt_pk_fp8_f32 v113, v100, v118
	v_mul_f32_e32 v114, 0x42800000, v20
	v_mul_f32_e32 v117, 0x42800000, v12
	v_cvt_pk_fp8_f32 v112, v114, v117 op_sel:[0,0,1]
	v_mul_f32_e32 v100, 0x42800000, v32
	v_mul_f32_e32 v114, 0x42800000, v16
	v_cvt_pk_fp8_f32 v113, v100, v114 op_sel:[0,0,1]
	v_mul_f32_e32 v100, 0x42800000, v9
	v_mul_f32_e32 v114, 0x42800000, v5
	v_mov_b32_e32 v119, 0
	v_cvt_pk_fp8_f32 v119, v100, v114
	v_mul_f32_e32 v100, 0x42800000, v29
	v_mul_f32_e32 v114, 0x42800000, v25
	v_mov_b32_e32 v120, 0
	v_cvt_pk_fp8_f32 v120, v100, v114
	s_mul_i32 s9, s21, 0x4100
	v_mul_f32_e32 v117, 0x42800000, v21
	v_mul_f32_e32 v118, 0x42800000, v13
	v_mul_f32_e32 v100, 0x42800000, v33
	v_mul_f32_e32 v114, 0x42800000, v17
	s_add_i32 s8, s4, -1
	s_add_i32 s9, s9, 0
	v_cvt_pk_fp8_f32 v119, v117, v118 op_sel:[0,0,1]
	v_cvt_pk_fp8_f32 v120, v100, v114 op_sel:[0,0,1]
	s_and_b32 s8, s10, s8
	v_add3_u32 v100, s9, v109, v103
	s_lshl_b32 s8, s8, 6
	ds_write2_b32 v100, v115, v116 offset0:65 offset1:66
	ds_write2_b64 v100, v[110:111], v[112:113] offset1:65
	ds_write2_b32 v100, v119, v120 offset0:195 offset1:196
	v_add_u32_e32 v100, s9, v98
	s_waitcnt lgkmcnt(0)
	s_barrier
	v_add_u32_e32 v112, v100, v105
	v_add_u32_e32 v114, s8, v104
	s_ff1_i32_b32 s4, s4
	ds_read2_b32 v[110:111], v112 offset1:1
	ds_read2_b32 v[112:113], v112 offset0:2 offset1:3
	v_ashrrev_i32_e32 v115, 31, v114
	s_lshr_b32 s4, s10, s4
	v_lshlrev_b64 v[114:115], 11, v[114:115]
	s_lshl_b32 s4, s4, 8
	v_lshl_add_u64 v[114:115], s[0:1], 0, v[114:115]
	v_lshl_add_u64 v[114:115], v[114:115], 0, s[4:5]
	v_lshl_add_u64 v[118:119], v[114:115], 0, v[98:99]
	v_add_u32_e32 v100, v100, v107
	ds_read2_b32 v[114:115], v100 offset1:1
	ds_read2_b32 v[116:117], v100 offset0:2 offset1:3
	s_waitcnt lgkmcnt(2)
	global_store_dwordx4 v[118:119], v[110:113], off nt
	s_nop 1
	v_add_u32_e32 v110, s8, v106
	v_ashrrev_i32_e32 v111, 31, v110
	v_lshlrev_b64 v[110:111], 11, v[110:111]
	v_lshl_add_u64 v[110:111], s[0:1], 0, v[110:111]
	v_lshl_add_u64 v[110:111], v[110:111], 0, s[4:5]
	s_add_i32 s4, s19, s3
	s_sub_i32 s24, s4, 40
	v_lshl_add_u64 v[110:111], v[110:111], 0, v[98:99]
	s_cmpk_gt_i32 s24, 0x5cff
	s_waitcnt lgkmcnt(0)
	global_store_dwordx4 v[110:111], v[114:117], off nt
	s_cbranch_scc1 .Lmy_c2_skip
	s_cmpk_lt_i32 s24, 0x4000
	s_cselect_b64 s[0:1], -1, 0
	s_cmpk_gt_i32 s24, 0x3fff
	s_mov_b64 s[10:11], -1
	s_cbranch_scc0 .LBB0_665
	s_addk_i32 s4, 0xbfd8
	s_lshr_b32 s4, s4, 8
	s_and_b32 s25, s24, 0xff
	s_lshl_b64 s[8:9], s[4:5], 24
	s_add_u32 s8, s76, s8
	s_addc_u32 s9, s77, s9
	s_mov_b64 s[10:11], 0

.LBB0_668:
	s_add_i32 s11, s4, -1
	s_and_b32 s11, s25, s11
	s_lshl_b32 s24, s11, 6
	v_or_b32_e32 v2, s24, v1
	v_bitop3_b32 v3, s24, v108, v1 bitop3:0xc8
	s_lshl_b32 s24, s25, 10
	s_lshl_b32 s11, s11, 5
	s_and_b32 s24, s24, 0x800
	s_and_b32 s11, s11, 0x3f80
	s_ff1_i32_b32 s4, s4
	s_add_i32 s11, s11, s24
	s_lshr_b32 s4, s25, s4
	v_or_b32_e32 v3, s11, v3
	v_cndmask_b32_e64 v100, v2, v3, s[0:1]
	v_lshl_add_u32 v2, s4, 8, v102
	v_mad_i64_i32 v[2:3], s[0:1], s10, v2, 0
	v_lshl_add_u64 v[2:3], v[2:3], 2, s[8:9]
	v_lshl_add_u64 v[2:3], v[100:101], 2, v[2:3]
	s_lshl_b32 s4, s10, 2
	v_lshl_add_u64 v[10:11], v[2:3], 0, s[4:5]
	global_load_dwordx4 v[6:9], v[2:3], off nt
	s_nop 0
	global_load_dwordx4 v[2:5], v[10:11], off nt
	v_lshl_add_u64 v[10:11], v[10:11], 0, s[4:5]
	v_lshl_add_u64 v[14:15], v[10:11], 0, s[4:5]
	global_load_dwordx4 v[18:21], v[10:11], off nt
	s_nop 0
	global_load_dwordx4 v[10:13], v[14:15], off nt
	v_lshl_add_u64 v[14:15], v[14:15], 0, s[4:5]
	v_lshl_add_u64 v[16:17], v[14:15], 0, s[4:5]
	global_load_dwordx4 v[26:29], v[14:15], off nt
	global_load_dwordx4 v[22:25], v[16:17], off nt
	v_lshl_add_u64 v[14:15], v[16:17], 0, s[4:5]
	v_lshl_add_u64 v[16:17], v[14:15], 0, s[4:5]
	global_load_dwordx4 v[30:33], v[14:15], off nt
	s_nop 0
	global_load_dwordx4 v[14:17], v[16:17], off nt
	s_waitcnt vmcnt(16)
	s_branch .LBB0_669
.Lmy_c2_skip:
	s_waitcnt vmcnt(0)
.LBB0_669:
	s_add_i32 s4, s17, s3
	s_xor_b32 s10, s21, 1
	s_sub_i32 s24, s4, 40
	s_cmpk_gt_i32 s24, 0x5cff
	s_cbranch_scc1 .LBB0_675
	s_cmpk_gt_i32 s24, 0x3fff
	s_mov_b64 s[8:9], -1
	s_cbranch_scc0 .LBB0_672
	s_addk_i32 s4, 0xbfd8
	s_lshr_b32 s4, s4, 8
	s_and_b32 s11, s24, 0xff
	s_lshl_b64 s[0:1], s[4:5], 22
	s_add_u32 s0, s13, s0
	s_addc_u32 s1, s14, s1
	s_mov_b64 s[8:9], 0

.LBB0_681:
	s_add_i32 s11, s4, -1
	s_and_b32 s11, s24, s11
	s_ff1_i32_b32 s4, s4
	s_lshl_b32 s25, s11, 6
	s_lshr_b32 s4, s24, s4
	s_lshl_b32 s24, s24, 10
	s_lshl_b32 s11, s11, 5
	s_and_b32 s24, s24, 0x800
	s_and_b32 s11, s11, 0x3f80
	v_bitop3_b32 v35, s25, v108, v1 bitop3:0xc8
	s_add_i32 s11, s11, s24
	v_or_b32_e32 v34, s25, v1
	v_or_b32_e32 v35, s11, v35
	v_cndmask_b32_e64 v100, v34, v35, s[0:1]
	v_lshl_add_u32 v34, s4, 8, v102
	v_mad_i64_i32 v[34:35], s[0:1], s10, v34, 0
	v_lshl_add_u64 v[34:35], v[34:35], 2, s[8:9]
	v_lshl_add_u64 v[34:35], v[100:101], 2, v[34:35]
	s_lshl_b32 s4, s10, 2
	v_lshl_add_u64 v[42:43], v[34:35], 0, s[4:5]
	global_load_dwordx4 v[34:37], v[34:35], off nt
	s_nop 0
	global_load_dwordx4 v[38:41], v[42:43], off nt
	v_lshl_add_u64 v[42:43], v[42:43], 0, s[4:5]
	v_lshl_add_u64 v[50:51], v[42:43], 0, s[4:5]
	global_load_dwordx4 v[42:45], v[42:43], off nt
	s_nop 0
	global_load_dwordx4 v[46:49], v[50:51], off nt
	v_lshl_add_u64 v[50:51], v[50:51], 0, s[4:5]
	v_lshl_add_u64 v[58:59], v[50:51], 0, s[4:5]
	global_load_dwordx4 v[50:53], v[50:51], off nt
	s_nop 0
	global_load_dwordx4 v[54:57], v[58:59], off nt
	v_lshl_add_u64 v[58:59], v[58:59], 0, s[4:5]
	v_lshl_add_u64 v[62:63], v[58:59], 0, s[4:5]
	global_load_dwordx4 v[58:61], v[58:59], off nt
	s_nop 0
	global_load_dwordx4 v[62:65], v[62:63], off nt
	s_waitcnt vmcnt(16)
	s_branch .LBB0_682
.Lmy_c3_skip:
	s_waitcnt vmcnt(0)
.LBB0_682:
	s_andn2_b64 vcc, exec, s[6:7]
	s_cbranch_vccnz .LBB0_650
	s_cmpk_gt_i32 s22, 0x3fff
	s_mov_b64 s[6:7], -1
	s_cbranch_scc0 .LBB0_685
	s_addk_i32 s23, 0xbfd8
	s_lshr_b32 s4, s23, 8
	s_and_b32 s8, s22, 0xff
	s_lshl_b64 s[0:1], s[4:5], 22
	s_add_u32 s0, s13, s0
	s_addc_u32 s1, s14, s1
	s_mov_b64 s[6:7], 0
